# in-projection K-loop: trailing half issues the next super-phase's staging loads between the MFMAs of its compute segment (one barrier interval earlier)
# baseline (speedup 1.0000x reference)
.LBB0_185:
	s_ashr_i32 s23, s22, 31
	s_lshl_b64 s[24:25], s[22:23], 19
	s_add_u32 s24, s19, s24
	s_addc_u32 s25, s33, s25
	s_and_b64 s[26:27], s[4:5], exec
	s_cselect_b32 s7, s25, s35
	s_cselect_b32 s9, s24, s34
	s_ashr_i32 s21, s20, 31
	s_lshl_b64 s[26:27], s[20:21], 19
	s_add_u32 s26, s38, s26
	s_addc_u32 s27, s39, s27
	s_and_b64 s[36:37], s[4:5], exec
	s_cselect_b32 s21, s27, s31
	s_cselect_b32 s23, s26, s30
	s_add_u32 s53, s30, 0x4000
	s_addc_u32 s54, s31, 0
	s_add_u32 s30, s34, 0x40080
	s_addc_u32 s31, s35, 0
	s_mov_b32 s55, -2
	ds_read_b128 v[26:29], v191
	ds_read_b128 v[30:33], v191 offset:1024
	ds_read_b128 v[18:21], v191 offset:2048
	ds_read_b128 v[22:25], v191 offset:3072
	ds_read_b128 v[10:13], v192
	ds_read_b128 v[14:17], v192 offset:1024
	ds_read_b128 v[2:5], v192 offset:2048
	ds_read_b128 v[6:9], v192 offset:3072
	ds_read_b128 v[196:199], v193
	ds_read_b128 v[200:203], v193 offset:1024
	ds_read_b128 v[204:207], v193 offset:2048
	ds_read_b128 v[208:211], v193 offset:3072
	ds_read_b128 v[212:215], v193 offset:4096
	ds_read_b128 v[216:219], v193 offset:5120
	ds_read_b128 v[220:223], v193 offset:6144
	ds_read_b128 v[224:227], v193 offset:7168
	s_add_u32 s0, s30, 0xfffc0080
	s_addc_u32 s1, s31, -1
	s_cmp_eq_u32 s55, 12
	s_cselect_b32 s37, s7, s1
	s_cselect_b32 s36, s9, s0
	s_cselect_b32 s35, s21, s54
	s_cselect_b32 s34, s23, s53
	v_lshl_add_u64 v[184:185], s[30:31], 0, v[176:177]
	s_add_i32 m0, s29, 0xc000
	s_nop 0
	global_load_lds_dwordx4 v[184:185], off
	v_lshl_add_u64 v[184:185], s[30:31], 0, v[178:179]
	s_add_i32 m0, s29, 0xe000
	s_nop 0
	global_load_lds_dwordx4 v[184:185], off
	s_and_b64 vcc, exec, s[14:15]
	s_cbranch_vccnz .Lwa_186p_0
	s_waitcnt vmcnt(8)
.Lwa_186p_0:
	s_waitcnt lgkmcnt(0)
	s_barrier
	s_setprio 1
	s_waitcnt lgkmcnt(0)
	v_mfma_scale_f32_16x16x128_f8f6f4 v[158:161], v[26:33], v[196:203], 0, v194, v194 op_sel_hi:[0,0,0]
	s_cbranch_vccnz .Leb_186p_18
	s_add_i32 s0, s49, s40
	v_lshl_add_u64 v[184:185], s[34:35], 0, v[164:165]
	s_mov_b32 m0, s0
	s_nop 0
	global_load_lds_dwordx4 v[184:185], off
.Leb_186p_18:
	v_mfma_scale_f32_16x16x128_f8f6f4 v[154:157], v[18:25], v[196:203], 0, v194, v194 op_sel_hi:[0,0,0]
	v_mfma_scale_f32_16x16x128_f8f6f4 v[142:145], v[26:33], v[204:211], 0, v194, v194 op_sel_hi:[0,0,0]
	s_cbranch_vccnz .Leb_186p_19
	s_add_i32 m0, s0, 0x2000
	s_add_u32 s56, s34, 0x40000
	v_lshl_add_u64 v[184:185], s[34:35], 0, v[168:169]
	s_addc_u32 s57, s35, 0
	s_add_i32 s0, s50, s40
	global_load_lds_dwordx4 v[184:185], off
.Leb_186p_19:
	v_mfma_scale_f32_16x16x128_f8f6f4 v[138:141], v[18:25], v[204:211], 0, v194, v194 op_sel_hi:[0,0,0]
	v_mfma_scale_f32_16x16x128_f8f6f4 v[126:129], v[26:33], v[212:219], 0, v194, v194 op_sel_hi:[0,0,0]
	s_cbranch_vccnz .Leb_186p_20
	v_lshl_add_u64 v[184:185], s[56:57], 0, v[164:165]
	s_mov_b32 m0, s0
	v_lshl_add_u64 v[186:187], s[36:37], 0, v[166:167]
	global_load_lds_dwordx4 v[184:185], off
.Leb_186p_20:
	v_mfma_scale_f32_16x16x128_f8f6f4 v[122:125], v[18:25], v[212:219], 0, v194, v194 op_sel_hi:[0,0,0]
	v_mfma_scale_f32_16x16x128_f8f6f4 v[110:113], v[26:33], v[220:227], 0, v194, v194 op_sel_hi:[0,0,0]
	s_cbranch_vccnz .Leb_186p_21
	v_lshl_add_u64 v[184:185], s[56:57], 0, v[168:169]
	s_add_i32 m0, s0, 0x2000
	s_nop 0
	global_load_lds_dwordx4 v[184:185], off
.Leb_186p_21:
	v_mfma_scale_f32_16x16x128_f8f6f4 v[106:109], v[18:25], v[220:227], 0, v194, v194 op_sel_hi:[0,0,0]
	s_setprio 0
	s_setprio 1
	v_mfma_scale_f32_16x16x128_f8f6f4 v[150:153], v[10:17], v[196:203], 0, v194, v194 op_sel_hi:[0,0,0]
	s_cbranch_vccnz .Leb_186p_22
	v_lshl_add_u64 v[184:185], s[36:37], 0, v[162:163]
	s_mov_b32 m0, s29
	s_nop 0
	global_load_lds_dwordx4 v[184:185], off
.Leb_186p_22:
	v_mfma_scale_f32_16x16x128_f8f6f4 v[146:149], v[2:9], v[196:203], 0, v194, v194 op_sel_hi:[0,0,0]
	v_mfma_scale_f32_16x16x128_f8f6f4 v[134:137], v[10:17], v[204:211], 0, v194, v194 op_sel_hi:[0,0,0]
	s_cbranch_vccnz .Leb_186p_23
	s_mov_b32 m0, s41
	s_nop 0
	global_load_lds_dwordx4 v[186:187], off
.Leb_186p_23:
	v_mfma_scale_f32_16x16x128_f8f6f4 v[130:133], v[2:9], v[204:211], 0, v194, v194 op_sel_hi:[0,0,0]
	v_mfma_scale_f32_16x16x128_f8f6f4 v[118:121], v[10:17], v[212:219], 0, v194, v194 op_sel_hi:[0,0,0]
	v_mfma_scale_f32_16x16x128_f8f6f4 v[114:117], v[2:9], v[212:219], 0, v194, v194 op_sel_hi:[0,0,0]
	v_mfma_scale_f32_16x16x128_f8f6f4 v[102:105], v[10:17], v[220:227], 0, v194, v194 op_sel_hi:[0,0,0]
	v_mfma_scale_f32_16x16x128_f8f6f4 v[98:101], v[2:9], v[220:227], 0, v194, v194 op_sel_hi:[0,0,0]
	s_cbranch_vccz .Lwb_186p_0
	s_waitcnt vmcnt(8)
.Lwb_186p_0:
	s_setprio 0
	s_barrier
	ds_read_b128 v[196:199], v193 offset:16384
	ds_read_b128 v[200:203], v193 offset:17408
	ds_read_b128 v[204:207], v193 offset:18432
	ds_read_b128 v[208:211], v193 offset:19456
	ds_read_b128 v[212:215], v193 offset:20480
	ds_read_b128 v[216:219], v193 offset:21504
	ds_read_b128 v[220:223], v193 offset:22528
	ds_read_b128 v[224:227], v193 offset:23552
	s_cbranch_vccz .Leb_186p_24
	s_add_i32 s0, s49, s40
	v_lshl_add_u64 v[184:185], s[34:35], 0, v[164:165]
	s_mov_b32 m0, s0
	s_nop 0
	global_load_lds_dwordx4 v[184:185], off
	s_add_i32 m0, s0, 0x2000
	s_add_u32 s56, s34, 0x40000
	v_lshl_add_u64 v[184:185], s[34:35], 0, v[168:169]
	s_addc_u32 s57, s35, 0
	s_add_i32 s0, s50, s40
	global_load_lds_dwordx4 v[184:185], off
	v_lshl_add_u64 v[184:185], s[56:57], 0, v[164:165]
	s_mov_b32 m0, s0
	v_lshl_add_u64 v[186:187], s[36:37], 0, v[166:167]
	global_load_lds_dwordx4 v[184:185], off
	v_lshl_add_u64 v[184:185], s[56:57], 0, v[168:169]
	s_add_i32 m0, s0, 0x2000
	s_nop 0
	global_load_lds_dwordx4 v[184:185], off
	v_lshl_add_u64 v[184:185], s[36:37], 0, v[162:163]
	s_mov_b32 m0, s29
	s_nop 0
	global_load_lds_dwordx4 v[184:185], off
	s_mov_b32 m0, s41
	s_nop 0
	global_load_lds_dwordx4 v[186:187], off
.Leb_186p_24:
	s_and_b64 vcc, exec, s[14:15]
	s_cbranch_vccnz .Lwa_186p_1
	s_waitcnt vmcnt(8)
.Lwa_186p_1:
	s_waitcnt lgkmcnt(0)
	s_barrier
	s_setprio 1
	s_waitcnt lgkmcnt(0)
	v_mfma_scale_f32_16x16x128_f8f6f4 v[94:97], v[26:33], v[196:203], 0, v194, v194 op_sel_hi:[0,0,0]
	v_mfma_scale_f32_16x16x128_f8f6f4 v[90:93], v[18:25], v[196:203], 0, v194, v194 op_sel_hi:[0,0,0]
	s_cbranch_vccnz .Leb_186p_25
	s_add_u32 s36, s36, 0x40000
	s_addc_u32 s37, s37, 0
	s_mov_b32 m0, s42
	v_lshl_add_u64 v[228:229], s[36:37], 0, v[162:163]
	global_load_lds_dwordx4 v[228:229], off
.Leb_186p_25:
	v_mfma_scale_f32_16x16x128_f8f6f4 v[78:81], v[26:33], v[204:211], 0, v194, v194 op_sel_hi:[0,0,0]
	v_mfma_scale_f32_16x16x128_f8f6f4 v[74:77], v[18:25], v[204:211], 0, v194, v194 op_sel_hi:[0,0,0]
	v_mfma_scale_f32_16x16x128_f8f6f4 v[62:65], v[26:33], v[212:219], 0, v194, v194 op_sel_hi:[0,0,0]
	v_mfma_scale_f32_16x16x128_f8f6f4 v[58:61], v[18:25], v[212:219], 0, v194, v194 op_sel_hi:[0,0,0]
	s_cbranch_vccnz .Leb_186p_26
	v_lshl_add_u64 v[228:229], s[36:37], 0, v[166:167]
	s_mov_b32 m0, s43
	s_nop 0
	global_load_lds_dwordx4 v[228:229], off
.Leb_186p_26:
	v_mfma_scale_f32_16x16x128_f8f6f4 v[46:49], v[26:33], v[220:227], 0, v194, v194 op_sel_hi:[0,0,0]
	v_mfma_scale_f32_16x16x128_f8f6f4 v[42:45], v[18:25], v[220:227], 0, v194, v194 op_sel_hi:[0,0,0]
	s_setprio 0
	s_setprio 1
	v_mfma_scale_f32_16x16x128_f8f6f4 v[86:89], v[10:17], v[196:203], 0, v194, v194 op_sel_hi:[0,0,0]
	v_mfma_scale_f32_16x16x128_f8f6f4 v[82:85], v[2:9], v[196:203], 0, v194, v194 op_sel_hi:[0,0,0]
	v_mfma_scale_f32_16x16x128_f8f6f4 v[70:73], v[10:17], v[204:211], 0, v194, v194 op_sel_hi:[0,0,0]
	v_mfma_scale_f32_16x16x128_f8f6f4 v[66:69], v[2:9], v[204:211], 0, v194, v194 op_sel_hi:[0,0,0]
	v_mfma_scale_f32_16x16x128_f8f6f4 v[54:57], v[10:17], v[212:219], 0, v194, v194 op_sel_hi:[0,0,0]
	v_mfma_scale_f32_16x16x128_f8f6f4 v[50:53], v[2:9], v[212:219], 0, v194, v194 op_sel_hi:[0,0,0]
	v_mfma_scale_f32_16x16x128_f8f6f4 v[38:41], v[10:17], v[220:227], 0, v194, v194 op_sel_hi:[0,0,0]
	v_mfma_scale_f32_16x16x128_f8f6f4 v[34:37], v[2:9], v[220:227], 0, v194, v194 op_sel_hi:[0,0,0]
	s_cbranch_vccz .Lwb_186p_1
	s_waitcnt vmcnt(8)

.LBB0_186:
	ds_read_b128 v[26:29], v191
	ds_read_b128 v[30:33], v191 offset:1024
	ds_read_b128 v[18:21], v191 offset:2048
	ds_read_b128 v[22:25], v191 offset:3072
	ds_read_b128 v[10:13], v192
	ds_read_b128 v[14:17], v192 offset:1024
	ds_read_b128 v[2:5], v192 offset:2048
	ds_read_b128 v[6:9], v192 offset:3072
	ds_read_b128 v[196:199], v193
	ds_read_b128 v[200:203], v193 offset:1024
	ds_read_b128 v[204:207], v193 offset:2048
	ds_read_b128 v[208:211], v193 offset:3072
	ds_read_b128 v[212:215], v193 offset:4096
	ds_read_b128 v[216:219], v193 offset:5120
	ds_read_b128 v[220:223], v193 offset:6144
	ds_read_b128 v[224:227], v193 offset:7168
	s_add_u32 s0, s30, 0xfffc0080
	s_addc_u32 s1, s31, -1
	s_cmp_eq_u32 s55, 12
	s_cselect_b32 s37, s7, s1
	s_cselect_b32 s36, s9, s0
	s_cselect_b32 s35, s21, s54
	s_cselect_b32 s34, s23, s53
	v_lshl_add_u64 v[184:185], s[30:31], 0, v[176:177]
	s_add_i32 m0, s29, 0xc000
	s_nop 0
	global_load_lds_dwordx4 v[184:185], off
	v_lshl_add_u64 v[184:185], s[30:31], 0, v[178:179]
	s_add_i32 m0, s29, 0xe000
	s_nop 0
	global_load_lds_dwordx4 v[184:185], off
	s_and_b64 vcc, exec, s[14:15]
	s_cbranch_vccnz .Lwa_186l_0
	s_waitcnt vmcnt(8)
.Lwa_186l_0:
	s_waitcnt lgkmcnt(0)
	s_barrier
	s_setprio 1
	s_waitcnt lgkmcnt(0)
	v_mfma_scale_f32_16x16x128_f8f6f4 v[158:161], v[26:33], v[196:203], v[158:161], v194, v194 op_sel_hi:[0,0,0]
	s_cbranch_vccnz .Leb_186_1
	s_add_i32 s0, s49, s40
	v_lshl_add_u64 v[184:185], s[34:35], 0, v[164:165]
	s_mov_b32 m0, s0
	s_nop 0
	global_load_lds_dwordx4 v[184:185], off
.Leb_186_1:
	v_mfma_scale_f32_16x16x128_f8f6f4 v[154:157], v[18:25], v[196:203], v[154:157], v194, v194 op_sel_hi:[0,0,0]
	v_mfma_scale_f32_16x16x128_f8f6f4 v[142:145], v[26:33], v[204:211], v[142:145], v194, v194 op_sel_hi:[0,0,0]
	s_cbranch_vccnz .Leb_186_2
	s_add_i32 m0, s0, 0x2000
	s_add_u32 s56, s34, 0x40000
	v_lshl_add_u64 v[184:185], s[34:35], 0, v[168:169]
	s_addc_u32 s57, s35, 0
	s_add_i32 s0, s50, s40
	global_load_lds_dwordx4 v[184:185], off
.Leb_186_2:
	v_mfma_scale_f32_16x16x128_f8f6f4 v[138:141], v[18:25], v[204:211], v[138:141], v194, v194 op_sel_hi:[0,0,0]
	v_mfma_scale_f32_16x16x128_f8f6f4 v[126:129], v[26:33], v[212:219], v[126:129], v194, v194 op_sel_hi:[0,0,0]
	s_cbranch_vccnz .Leb_186_3
	v_lshl_add_u64 v[184:185], s[56:57], 0, v[164:165]
	s_mov_b32 m0, s0
	v_lshl_add_u64 v[186:187], s[36:37], 0, v[166:167]
	global_load_lds_dwordx4 v[184:185], off
.Leb_186_3:
	v_mfma_scale_f32_16x16x128_f8f6f4 v[122:125], v[18:25], v[212:219], v[122:125], v194, v194 op_sel_hi:[0,0,0]
	v_mfma_scale_f32_16x16x128_f8f6f4 v[110:113], v[26:33], v[220:227], v[110:113], v194, v194 op_sel_hi:[0,0,0]
	s_cbranch_vccnz .Leb_186_4
	v_lshl_add_u64 v[184:185], s[56:57], 0, v[168:169]
	s_add_i32 m0, s0, 0x2000
	s_nop 0
	global_load_lds_dwordx4 v[184:185], off
.Leb_186_4:
	v_mfma_scale_f32_16x16x128_f8f6f4 v[106:109], v[18:25], v[220:227], v[106:109], v194, v194 op_sel_hi:[0,0,0]
	s_setprio 0
	s_setprio 1
	v_mfma_scale_f32_16x16x128_f8f6f4 v[150:153], v[10:17], v[196:203], v[150:153], v194, v194 op_sel_hi:[0,0,0]
	s_cbranch_vccnz .Leb_186_5
	v_lshl_add_u64 v[184:185], s[36:37], 0, v[162:163]
	s_mov_b32 m0, s29
	s_nop 0
	global_load_lds_dwordx4 v[184:185], off
.Leb_186_5:
	v_mfma_scale_f32_16x16x128_f8f6f4 v[146:149], v[2:9], v[196:203], v[146:149], v194, v194 op_sel_hi:[0,0,0]
	v_mfma_scale_f32_16x16x128_f8f6f4 v[134:137], v[10:17], v[204:211], v[134:137], v194, v194 op_sel_hi:[0,0,0]
	s_cbranch_vccnz .Leb_186_6
	s_mov_b32 m0, s41
	s_nop 0
	global_load_lds_dwordx4 v[186:187], off
.Leb_186_6:
	v_mfma_scale_f32_16x16x128_f8f6f4 v[130:133], v[2:9], v[204:211], v[130:133], v194, v194 op_sel_hi:[0,0,0]
	v_mfma_scale_f32_16x16x128_f8f6f4 v[118:121], v[10:17], v[212:219], v[118:121], v194, v194 op_sel_hi:[0,0,0]
	v_mfma_scale_f32_16x16x128_f8f6f4 v[114:117], v[2:9], v[212:219], v[114:117], v194, v194 op_sel_hi:[0,0,0]
	v_mfma_scale_f32_16x16x128_f8f6f4 v[102:105], v[10:17], v[220:227], v[102:105], v194, v194 op_sel_hi:[0,0,0]
	v_mfma_scale_f32_16x16x128_f8f6f4 v[98:101], v[2:9], v[220:227], v[98:101], v194, v194 op_sel_hi:[0,0,0]
	s_cbranch_vccz .Lwb_186l_0
	s_waitcnt vmcnt(8)

.Lwa_186l_1:
	s_waitcnt lgkmcnt(0)
	s_barrier
	s_setprio 1
	s_waitcnt lgkmcnt(0)
	v_mfma_scale_f32_16x16x128_f8f6f4 v[94:97], v[26:33], v[196:203], v[94:97], v194, v194 op_sel_hi:[0,0,0]
	v_mfma_scale_f32_16x16x128_f8f6f4 v[90:93], v[18:25], v[196:203], v[90:93], v194, v194 op_sel_hi:[0,0,0]
	s_cbranch_vccnz .Leb_186_8
	s_add_u32 s36, s36, 0x40000
	s_addc_u32 s37, s37, 0
	s_mov_b32 m0, s42
	v_lshl_add_u64 v[228:229], s[36:37], 0, v[162:163]
	global_load_lds_dwordx4 v[228:229], off
.Leb_186_8:
	v_mfma_scale_f32_16x16x128_f8f6f4 v[78:81], v[26:33], v[204:211], v[78:81], v194, v194 op_sel_hi:[0,0,0]
	v_mfma_scale_f32_16x16x128_f8f6f4 v[74:77], v[18:25], v[204:211], v[74:77], v194, v194 op_sel_hi:[0,0,0]
	v_mfma_scale_f32_16x16x128_f8f6f4 v[62:65], v[26:33], v[212:219], v[62:65], v194, v194 op_sel_hi:[0,0,0]
	v_mfma_scale_f32_16x16x128_f8f6f4 v[58:61], v[18:25], v[212:219], v[58:61], v194, v194 op_sel_hi:[0,0,0]
	s_cbranch_vccnz .Leb_186_9
	v_lshl_add_u64 v[228:229], s[36:37], 0, v[166:167]
	s_mov_b32 m0, s43
	s_nop 0
	global_load_lds_dwordx4 v[228:229], off
.Leb_186_9:
	v_mfma_scale_f32_16x16x128_f8f6f4 v[46:49], v[26:33], v[220:227], v[46:49], v194, v194 op_sel_hi:[0,0,0]
	v_mfma_scale_f32_16x16x128_f8f6f4 v[42:45], v[18:25], v[220:227], v[42:45], v194, v194 op_sel_hi:[0,0,0]
	s_setprio 0
	s_setprio 1
	v_mfma_scale_f32_16x16x128_f8f6f4 v[86:89], v[10:17], v[196:203], v[86:89], v194, v194 op_sel_hi:[0,0,0]
	v_mfma_scale_f32_16x16x128_f8f6f4 v[82:85], v[2:9], v[196:203], v[82:85], v194, v194 op_sel_hi:[0,0,0]
	v_mfma_scale_f32_16x16x128_f8f6f4 v[70:73], v[10:17], v[204:211], v[70:73], v194, v194 op_sel_hi:[0,0,0]
	v_mfma_scale_f32_16x16x128_f8f6f4 v[66:69], v[2:9], v[204:211], v[66:69], v194, v194 op_sel_hi:[0,0,0]
	v_mfma_scale_f32_16x16x128_f8f6f4 v[54:57], v[10:17], v[212:219], v[54:57], v194, v194 op_sel_hi:[0,0,0]
	v_mfma_scale_f32_16x16x128_f8f6f4 v[50:53], v[2:9], v[212:219], v[50:53], v194, v194 op_sel_hi:[0,0,0]
	v_mfma_scale_f32_16x16x128_f8f6f4 v[38:41], v[10:17], v[220:227], v[38:41], v194, v194 op_sel_hi:[0,0,0]
	v_mfma_scale_f32_16x16x128_f8f6f4 v[34:37], v[2:9], v[220:227], v[34:37], v194, v194 op_sel_hi:[0,0,0]
	s_cbranch_vccz .Lwb_186l_1
	s_waitcnt vmcnt(8)

.Lmid_186:
	s_add_i32 s0, 0, 0x18000
	v_add_u32_e32 v0, s0, v189
	s_add_i32 s1, 0, 0x1c000
	ds_read_b128 v[2:5], v0
	ds_read_b128 v[6:9], v0 offset:1024
	ds_read_b128 v[10:13], v0 offset:2048
	ds_read_b128 v[14:17], v0 offset:3072
	v_add_u32_e32 v0, s1, v189
	ds_read_b128 v[18:21], v0
	ds_read_b128 v[22:25], v0 offset:1024
	ds_read_b128 v[26:29], v0 offset:2048
	ds_read_b128 v[30:33], v0 offset:3072
	ds_read_b128 v[196:199], v193 offset:32768
	ds_read_b128 v[200:203], v193 offset:33792
	ds_read_b128 v[204:207], v193 offset:34816
	ds_read_b128 v[208:211], v193 offset:35840
	ds_read_b128 v[212:215], v193 offset:36864
	ds_read_b128 v[216:219], v193 offset:37888
	ds_read_b128 v[220:223], v193 offset:38912
	ds_read_b128 v[224:227], v193 offset:39936
	s_cbranch_vccz .Leb_186_10
	s_add_u32 s36, s36, 0x40000
	s_addc_u32 s37, s37, 0
	s_mov_b32 m0, s42
	v_lshl_add_u64 v[228:229], s[36:37], 0, v[162:163]
	global_load_lds_dwordx4 v[228:229], off
	v_lshl_add_u64 v[228:229], s[36:37], 0, v[166:167]
	s_mov_b32 m0, s43
	s_nop 0
	global_load_lds_dwordx4 v[228:229], off

.Lwa_186l_2:
	s_waitcnt lgkmcnt(0)
	s_barrier
	s_setprio 1
	s_waitcnt lgkmcnt(0)
	v_mfma_scale_f32_16x16x128_f8f6f4 v[158:161], v[2:9], v[196:203], v[158:161], v194, v194 op_sel_hi:[0,0,0]
	s_cbranch_vccnz .Leb_186_11
	s_add_u32 s36, s34, 0x2000
	s_addc_u32 s37, s35, 0
	s_add_i32 s0, s0, s40
	v_lshl_add_u64 v[228:229], s[36:37], 0, v[164:165]
	s_mov_b32 m0, s0
	s_nop 0
	global_load_lds_dwordx4 v[228:229], off
.Leb_186_11:
	v_mfma_scale_f32_16x16x128_f8f6f4 v[154:157], v[10:17], v[196:203], v[154:157], v194, v194 op_sel_hi:[0,0,0]
	v_mfma_scale_f32_16x16x128_f8f6f4 v[142:145], v[2:9], v[204:211], v[142:145], v194, v194 op_sel_hi:[0,0,0]
	s_cbranch_vccnz .Leb_186_12
	s_add_i32 m0, s0, 0x2000
	s_add_u32 s34, s34, 0x42000
	v_lshl_add_u64 v[228:229], s[36:37], 0, v[168:169]
	s_addc_u32 s35, s35, 0
	s_add_i32 s0, s1, s40
	global_load_lds_dwordx4 v[228:229], off
.Leb_186_12:
	v_mfma_scale_f32_16x16x128_f8f6f4 v[138:141], v[10:17], v[204:211], v[138:141], v194, v194 op_sel_hi:[0,0,0]
	v_mfma_scale_f32_16x16x128_f8f6f4 v[126:129], v[2:9], v[212:219], v[126:129], v194, v194 op_sel_hi:[0,0,0]
	s_cbranch_vccnz .Leb_186_13
	v_lshl_add_u64 v[228:229], s[34:35], 0, v[164:165]
	s_mov_b32 m0, s0
	v_lshl_add_u64 v[184:185], v[184:185], 0, s[12:13]
	global_load_lds_dwordx4 v[228:229], off
.Leb_186_13:
	v_mfma_scale_f32_16x16x128_f8f6f4 v[122:125], v[10:17], v[212:219], v[122:125], v194, v194 op_sel_hi:[0,0,0]
	v_mfma_scale_f32_16x16x128_f8f6f4 v[110:113], v[2:9], v[220:227], v[110:113], v194, v194 op_sel_hi:[0,0,0]
	s_cbranch_vccnz .Leb_186_14
	v_lshl_add_u64 v[228:229], s[34:35], 0, v[168:169]
	s_add_i32 m0, s0, 0x2000
	s_nop 0
	global_load_lds_dwordx4 v[228:229], off
.Leb_186_14:
	v_mfma_scale_f32_16x16x128_f8f6f4 v[106:109], v[10:17], v[220:227], v[106:109], v194, v194 op_sel_hi:[0,0,0]
	s_setprio 0
	s_setprio 1
	v_mfma_scale_f32_16x16x128_f8f6f4 v[150:153], v[18:25], v[196:203], v[150:153], v194, v194 op_sel_hi:[0,0,0]
	s_cbranch_vccnz .Leb_186_15
	s_mov_b32 m0, s44
	s_nop 0
	global_load_lds_dwordx4 v[184:185], off
.Leb_186_15:
	v_mfma_scale_f32_16x16x128_f8f6f4 v[146:149], v[26:33], v[196:203], v[146:149], v194, v194 op_sel_hi:[0,0,0]
	v_mfma_scale_f32_16x16x128_f8f6f4 v[134:137], v[18:25], v[204:211], v[134:137], v194, v194 op_sel_hi:[0,0,0]
	s_cbranch_vccnz .Leb_186_16
	v_lshl_add_u64 v[184:185], v[186:187], 0, s[12:13]
	s_mov_b32 m0, s45
	s_nop 0
	global_load_lds_dwordx4 v[184:185], off
.Leb_186_16:
	v_mfma_scale_f32_16x16x128_f8f6f4 v[130:133], v[26:33], v[204:211], v[130:133], v194, v194 op_sel_hi:[0,0,0]
	v_mfma_scale_f32_16x16x128_f8f6f4 v[118:121], v[18:25], v[212:219], v[118:121], v194, v194 op_sel_hi:[0,0,0]
	v_mfma_scale_f32_16x16x128_f8f6f4 v[114:117], v[26:33], v[212:219], v[114:117], v194, v194 op_sel_hi:[0,0,0]
	v_mfma_scale_f32_16x16x128_f8f6f4 v[102:105], v[18:25], v[220:227], v[102:105], v194, v194 op_sel_hi:[0,0,0]
	v_mfma_scale_f32_16x16x128_f8f6f4 v[98:101], v[26:33], v[220:227], v[98:101], v194, v194 op_sel_hi:[0,0,0]
	s_cbranch_vccz .Lwb_186l_2
	s_waitcnt vmcnt(8)
.Lwb_186l_2:
	s_setprio 0
	s_barrier
	ds_read_b128 v[196:199], v193 offset:49152
	ds_read_b128 v[200:203], v193 offset:50176
	ds_read_b128 v[204:207], v193 offset:51200
	ds_read_b128 v[208:211], v193 offset:52224
	ds_read_b128 v[212:215], v193 offset:53248
	ds_read_b128 v[216:219], v193 offset:54272
	ds_read_b128 v[220:223], v193 offset:55296
	ds_read_b128 v[224:227], v193 offset:56320
	s_cbranch_vccz .Leb_186_17
	s_add_u32 s36, s34, 0x2000
	s_addc_u32 s37, s35, 0
	s_add_i32 s0, s0, s40
	v_lshl_add_u64 v[228:229], s[36:37], 0, v[164:165]
	s_mov_b32 m0, s0
	s_nop 0
	global_load_lds_dwordx4 v[228:229], off
	s_add_i32 m0, s0, 0x2000
	s_add_u32 s34, s34, 0x42000
	v_lshl_add_u64 v[228:229], s[36:37], 0, v[168:169]
	s_addc_u32 s35, s35, 0
	s_add_i32 s0, s1, s40
	global_load_lds_dwordx4 v[228:229], off
	v_lshl_add_u64 v[228:229], s[34:35], 0, v[164:165]
	s_mov_b32 m0, s0
	v_lshl_add_u64 v[184:185], v[184:185], 0, s[12:13]
	global_load_lds_dwordx4 v[228:229], off
	v_lshl_add_u64 v[228:229], s[34:35], 0, v[168:169]
	s_add_i32 m0, s0, 0x2000
	s_nop 0
	global_load_lds_dwordx4 v[228:229], off
	s_mov_b32 m0, s44
	s_nop 0
	global_load_lds_dwordx4 v[184:185], off
	v_lshl_add_u64 v[184:185], v[186:187], 0, s[12:13]
	s_mov_b32 m0, s45
	s_nop 0
	global_load_lds_dwordx4 v[184:185], off
